# shadow conversion queue: next-chunk atomic waited at the end of the chunk instead of right after the request
# speedup vs baseline: 1.0336x; 1.0006x over previous
.LBB0_123:
	ds_read_b128 v[156:159], v152
	ds_read_b128 v[160:163], v152 offset:1024
	ds_read_b128 v[164:167], v152 offset:2048
	ds_read_b128 v[168:171], v152 offset:3072
	ds_read_b128 v[172:175], v153
	ds_read_b128 v[176:179], v153 offset:1024
	ds_read_b128 v[180:183], v153 offset:2048
	ds_read_b128 v[184:187], v153 offset:3072
	s_add_u32 s20, s26, 0xfffc0080
	s_addc_u32 s21, s27, -1
	s_cmp_eq_u32 s97, 12
	s_cselect_b32 s29, s17, s21
	s_cselect_b32 s28, s92, s20
	s_cselect_b32 s21, s15, s96
	s_cselect_b32 s20, s93, s95
	v_lshl_add_u64 v[148:149], s[26:27], 0, v[138:139]
	s_add_i32 m0, s25, 0xc000
	ds_read_b128 v[188:191], v154
	ds_read_b128 v[192:195], v154 offset:1024
	ds_read_b128 v[196:199], v154 offset:2048
	ds_read_b128 v[200:203], v154 offset:3072
	ds_read_b128 v[204:207], v154 offset:4096
	ds_read_b128 v[208:211], v154 offset:5120
	ds_read_b128 v[212:215], v154 offset:6144
	ds_read_b128 v[216:219], v154 offset:7168
	global_load_lds_dwordx4 v[148:149], off
	v_lshl_add_u64 v[148:149], s[26:27], 0, v[140:141]
	s_add_i32 m0, s25, 0xe000
	s_nop 0
	global_load_lds_dwordx4 v[148:149], off
	s_waitcnt vmcnt(8)
	s_waitcnt lgkmcnt(0)
	s_barrier
	s_cmp_eq_u32 s97, 12
	s_cbranch_scc0 .Lp1_noepf
	v_lshl_add_u32 v228, s24, 8, v147
	v_lshlrev_b32_e32 v228, 2, v228
	global_load_dword v238, v228, s[8:9]
	global_load_dword v239, v228, s[8:9] offset:64
	global_load_dword v240, v228, s[8:9] offset:128
	global_load_dword v241, v228, s[8:9] offset:192
	global_load_dword v242, v228, s[8:9] offset:512
	global_load_dword v243, v228, s[8:9] offset:576
	global_load_dword v244, v228, s[8:9] offset:640
	global_load_dword v245, v228, s[8:9] offset:704
.Lp1_noepf:
	s_setprio 1
	s_waitcnt lgkmcnt(0)
	v_mfma_f32_16x16x32_bf16 v[124:127], v[156:159], v[188:191], v[124:127]
	v_mfma_f32_16x16x32_bf16 v[120:123], v[164:167], v[188:191], v[120:123]
	v_mfma_f32_16x16x32_bf16 v[116:119], v[156:159], v[196:199], v[116:119]
	v_mfma_f32_16x16x32_bf16 v[112:115], v[164:167], v[196:199], v[112:115]
	v_mfma_f32_16x16x32_bf16 v[100:103], v[156:159], v[204:207], v[100:103]
	v_mfma_f32_16x16x32_bf16 v[96:99], v[164:167], v[204:207], v[96:99]
	v_mfma_f32_16x16x32_bf16 v[76:79], v[156:159], v[212:215], v[76:79]
	v_mfma_f32_16x16x32_bf16 v[72:75], v[164:167], v[212:215], v[72:75]
	v_mfma_f32_16x16x32_bf16 v[124:127], v[160:163], v[192:195], v[124:127]
	v_mfma_f32_16x16x32_bf16 v[120:123], v[168:171], v[192:195], v[120:123]
	v_mfma_f32_16x16x32_bf16 v[116:119], v[160:163], v[200:203], v[116:119]
	v_mfma_f32_16x16x32_bf16 v[112:115], v[168:171], v[200:203], v[112:115]
	v_mfma_f32_16x16x32_bf16 v[100:103], v[160:163], v[208:211], v[100:103]
	v_mfma_f32_16x16x32_bf16 v[96:99], v[168:171], v[208:211], v[96:99]
	v_mfma_f32_16x16x32_bf16 v[76:79], v[160:163], v[216:219], v[76:79]
	v_mfma_f32_16x16x32_bf16 v[72:75], v[168:171], v[216:219], v[72:75]
	s_setprio 0
	s_setprio 1
	v_mfma_f32_16x16x32_bf16 v[108:111], v[172:175], v[188:191], v[108:111]
	v_mfma_f32_16x16x32_bf16 v[104:107], v[180:183], v[188:191], v[104:107]
	v_mfma_f32_16x16x32_bf16 v[92:95], v[172:175], v[196:199], v[92:95]
	v_mfma_f32_16x16x32_bf16 v[88:91], v[180:183], v[196:199], v[88:91]
	v_mfma_f32_16x16x32_bf16 v[84:87], v[172:175], v[204:207], v[84:87]
	v_mfma_f32_16x16x32_bf16 v[80:83], v[180:183], v[204:207], v[80:83]
	v_mfma_f32_16x16x32_bf16 v[68:71], v[172:175], v[212:215], v[68:71]
	v_mfma_f32_16x16x32_bf16 v[64:67], v[180:183], v[212:215], v[64:67]
	v_mfma_f32_16x16x32_bf16 v[108:111], v[176:179], v[192:195], v[108:111]
	v_mfma_f32_16x16x32_bf16 v[104:107], v[184:187], v[192:195], v[104:107]
	v_mfma_f32_16x16x32_bf16 v[92:95], v[176:179], v[200:203], v[92:95]
	v_mfma_f32_16x16x32_bf16 v[88:91], v[184:187], v[200:203], v[88:91]
	v_mfma_f32_16x16x32_bf16 v[84:87], v[176:179], v[208:211], v[84:87]
	v_mfma_f32_16x16x32_bf16 v[80:83], v[184:187], v[208:211], v[80:83]
	v_mfma_f32_16x16x32_bf16 v[68:71], v[176:179], v[216:219], v[68:71]
	v_mfma_f32_16x16x32_bf16 v[64:67], v[184:187], v[216:219], v[64:67]
	s_setprio 0
	s_barrier
	s_add_i32 vcc_lo, s75, s40
	v_lshl_add_u64 v[148:149], s[20:21], 0, v[130:131]
	s_mov_b32 m0, vcc_lo
	ds_read_b128 v[188:191], v154 offset:16384
	ds_read_b128 v[192:195], v154 offset:17408
	ds_read_b128 v[196:199], v154 offset:18432
	ds_read_b128 v[200:203], v154 offset:19456
	ds_read_b128 v[204:207], v154 offset:20480
	ds_read_b128 v[208:211], v154 offset:21504
	ds_read_b128 v[212:215], v154 offset:22528
	ds_read_b128 v[216:219], v154 offset:23552
	global_load_lds_dwordx4 v[148:149], off
	s_add_i32 m0, vcc_lo, 0x2000
	s_add_u32 vcc_lo, s20, 0x40000
	v_lshl_add_u64 v[220:221], s[20:21], 0, v[134:135]
	s_addc_u32 vcc_hi, s21, 0
	s_add_i32 s44, s80, s40
	global_load_lds_dwordx4 v[220:221], off
	v_lshl_add_u64 v[222:223], vcc, 0, v[130:131]
	s_mov_b32 m0, s44
	v_lshl_add_u64 v[224:225], s[28:29], 0, v[132:133]
	global_load_lds_dwordx4 v[222:223], off
	v_lshl_add_u64 v[222:223], vcc, 0, v[134:135]
	s_add_i32 m0, s44, 0x2000
	s_nop 0
	global_load_lds_dwordx4 v[222:223], off
	v_lshl_add_u64 v[222:223], s[28:29], 0, v[128:129]
	s_mov_b32 m0, s25
	s_nop 0
	global_load_lds_dwordx4 v[222:223], off
	s_mov_b32 m0, s45
	s_nop 0
	global_load_lds_dwordx4 v[224:225], off
	s_waitcnt vmcnt(8)
	s_waitcnt lgkmcnt(0)
	s_barrier
	s_setprio 1
	s_waitcnt lgkmcnt(0)
	v_mfma_f32_16x16x32_bf16 v[60:63], v[156:159], v[188:191], v[60:63]
	v_mfma_f32_16x16x32_bf16 v[56:59], v[164:167], v[188:191], v[56:59]
	v_mfma_f32_16x16x32_bf16 v[52:55], v[156:159], v[196:199], v[52:55]
	v_mfma_f32_16x16x32_bf16 v[44:47], v[164:167], v[196:199], v[44:47]
	v_mfma_f32_16x16x32_bf16 v[36:39], v[156:159], v[204:207], v[36:39]
	v_mfma_f32_16x16x32_bf16 v[28:31], v[164:167], v[204:207], v[28:31]
	v_mfma_f32_16x16x32_bf16 v[20:23], v[156:159], v[212:215], v[20:23]
	v_mfma_f32_16x16x32_bf16 v[12:15], v[164:167], v[212:215], v[12:15]
	v_mfma_f32_16x16x32_bf16 v[60:63], v[160:163], v[192:195], v[60:63]
	v_mfma_f32_16x16x32_bf16 v[56:59], v[168:171], v[192:195], v[56:59]
	v_mfma_f32_16x16x32_bf16 v[52:55], v[160:163], v[200:203], v[52:55]
	v_mfma_f32_16x16x32_bf16 v[44:47], v[168:171], v[200:203], v[44:47]
	v_mfma_f32_16x16x32_bf16 v[36:39], v[160:163], v[208:211], v[36:39]
	v_mfma_f32_16x16x32_bf16 v[28:31], v[168:171], v[208:211], v[28:31]
	v_mfma_f32_16x16x32_bf16 v[20:23], v[160:163], v[216:219], v[20:23]
	v_mfma_f32_16x16x32_bf16 v[12:15], v[168:171], v[216:219], v[12:15]
	s_setprio 0
	s_setprio 1
	v_mfma_f32_16x16x32_bf16 v[48:51], v[172:175], v[188:191], v[48:51]
	v_mfma_f32_16x16x32_bf16 v[40:43], v[180:183], v[188:191], v[40:43]
	v_mfma_f32_16x16x32_bf16 v[32:35], v[172:175], v[196:199], v[32:35]
	v_mfma_f32_16x16x32_bf16 v[24:27], v[180:183], v[196:199], v[24:27]
	v_mfma_f32_16x16x32_bf16 v[16:19], v[172:175], v[204:207], v[16:19]
	v_mfma_f32_16x16x32_bf16 v[8:11], v[180:183], v[204:207], v[8:11]
	v_mfma_f32_16x16x32_bf16 v[4:7], v[172:175], v[212:215], v[4:7]
	v_mfma_f32_16x16x32_bf16 v[0:3], v[180:183], v[212:215], v[0:3]
	v_mfma_f32_16x16x32_bf16 v[48:51], v[176:179], v[192:195], v[48:51]
	v_mfma_f32_16x16x32_bf16 v[40:43], v[184:187], v[192:195], v[40:43]
	v_mfma_f32_16x16x32_bf16 v[32:35], v[176:179], v[200:203], v[32:35]
	v_mfma_f32_16x16x32_bf16 v[24:27], v[184:187], v[200:203], v[24:27]
	v_mfma_f32_16x16x32_bf16 v[16:19], v[176:179], v[208:211], v[16:19]
	v_mfma_f32_16x16x32_bf16 v[8:11], v[184:187], v[208:211], v[8:11]
	v_mfma_f32_16x16x32_bf16 v[4:7], v[176:179], v[216:219], v[4:7]
	v_mfma_f32_16x16x32_bf16 v[0:3], v[184:187], v[216:219], v[0:3]
	s_setprio 0
	s_barrier
	s_add_i32 s44, 0, 0x18000
	v_add_u32_e32 v136, s44, v150
	s_add_i32 vcc_lo, 0, 0x1c000
	ds_read_b128 v[156:159], v136
	ds_read_b128 v[160:163], v136 offset:1024
	ds_read_b128 v[164:167], v136 offset:2048
	ds_read_b128 v[168:171], v136 offset:3072
	v_add_u32_e32 v136, vcc_lo, v150
	ds_read_b128 v[172:175], v136
	ds_read_b128 v[176:179], v136 offset:1024
	ds_read_b128 v[180:183], v136 offset:2048
	ds_read_b128 v[184:187], v136 offset:3072
	s_add_u32 s28, s28, 0x40000
	s_addc_u32 s29, s29, 0
	s_mov_b32 m0, s52
	v_lshl_add_u64 v[226:227], s[28:29], 0, v[128:129]
	ds_read_b128 v[188:191], v154 offset:32768
	ds_read_b128 v[192:195], v154 offset:33792
	ds_read_b128 v[196:199], v154 offset:34816
	ds_read_b128 v[200:203], v154 offset:35840
	ds_read_b128 v[204:207], v154 offset:36864
	ds_read_b128 v[208:211], v154 offset:37888
	ds_read_b128 v[212:215], v154 offset:38912
	ds_read_b128 v[216:219], v154 offset:39936
	global_load_lds_dwordx4 v[226:227], off
	v_lshl_add_u64 v[226:227], s[28:29], 0, v[132:133]
	s_mov_b32 m0, s53
	s_nop 0
	global_load_lds_dwordx4 v[226:227], off
	s_waitcnt vmcnt(8)
	s_waitcnt lgkmcnt(0)
	s_barrier
	s_setprio 1
	s_waitcnt lgkmcnt(0)
	v_mfma_f32_16x16x32_bf16 v[124:127], v[156:159], v[188:191], v[124:127]
	v_mfma_f32_16x16x32_bf16 v[120:123], v[164:167], v[188:191], v[120:123]
	v_mfma_f32_16x16x32_bf16 v[116:119], v[156:159], v[196:199], v[116:119]
	v_mfma_f32_16x16x32_bf16 v[112:115], v[164:167], v[196:199], v[112:115]
	v_mfma_f32_16x16x32_bf16 v[100:103], v[156:159], v[204:207], v[100:103]
	v_mfma_f32_16x16x32_bf16 v[96:99], v[164:167], v[204:207], v[96:99]
	v_mfma_f32_16x16x32_bf16 v[76:79], v[156:159], v[212:215], v[76:79]
	v_mfma_f32_16x16x32_bf16 v[72:75], v[164:167], v[212:215], v[72:75]
	v_mfma_f32_16x16x32_bf16 v[124:127], v[160:163], v[192:195], v[124:127]
	v_mfma_f32_16x16x32_bf16 v[120:123], v[168:171], v[192:195], v[120:123]
	v_mfma_f32_16x16x32_bf16 v[116:119], v[160:163], v[200:203], v[116:119]
	v_mfma_f32_16x16x32_bf16 v[112:115], v[168:171], v[200:203], v[112:115]
	v_mfma_f32_16x16x32_bf16 v[100:103], v[160:163], v[208:211], v[100:103]
	v_mfma_f32_16x16x32_bf16 v[96:99], v[168:171], v[208:211], v[96:99]
	v_mfma_f32_16x16x32_bf16 v[76:79], v[160:163], v[216:219], v[76:79]
	v_mfma_f32_16x16x32_bf16 v[72:75], v[168:171], v[216:219], v[72:75]
	s_setprio 0
	s_setprio 1
	v_mfma_f32_16x16x32_bf16 v[108:111], v[172:175], v[188:191], v[108:111]
	v_mfma_f32_16x16x32_bf16 v[104:107], v[180:183], v[188:191], v[104:107]
	v_mfma_f32_16x16x32_bf16 v[92:95], v[172:175], v[196:199], v[92:95]
	v_mfma_f32_16x16x32_bf16 v[88:91], v[180:183], v[196:199], v[88:91]
	v_mfma_f32_16x16x32_bf16 v[84:87], v[172:175], v[204:207], v[84:87]
	v_mfma_f32_16x16x32_bf16 v[80:83], v[180:183], v[204:207], v[80:83]
	v_mfma_f32_16x16x32_bf16 v[68:71], v[172:175], v[212:215], v[68:71]
	v_mfma_f32_16x16x32_bf16 v[64:67], v[180:183], v[212:215], v[64:67]
	v_mfma_f32_16x16x32_bf16 v[108:111], v[176:179], v[192:195], v[108:111]
	v_mfma_f32_16x16x32_bf16 v[104:107], v[184:187], v[192:195], v[104:107]
	v_mfma_f32_16x16x32_bf16 v[92:95], v[176:179], v[200:203], v[92:95]
	v_mfma_f32_16x16x32_bf16 v[88:91], v[184:187], v[200:203], v[88:91]
	v_mfma_f32_16x16x32_bf16 v[84:87], v[176:179], v[208:211], v[84:87]
	v_mfma_f32_16x16x32_bf16 v[80:83], v[184:187], v[208:211], v[80:83]
	v_mfma_f32_16x16x32_bf16 v[68:71], v[176:179], v[216:219], v[68:71]
	v_mfma_f32_16x16x32_bf16 v[64:67], v[184:187], v[216:219], v[64:67]
	s_setprio 0
	s_barrier
	s_add_i32 s28, s44, s40
	v_lshl_add_u64 v[148:149], v[148:149], 0, s[10:11]
	s_mov_b32 m0, s28
	ds_read_b128 v[188:191], v154 offset:49152
	ds_read_b128 v[192:195], v154 offset:50176
	ds_read_b128 v[196:199], v154 offset:51200
	ds_read_b128 v[200:203], v154 offset:52224
	ds_read_b128 v[204:207], v154 offset:53248
	ds_read_b128 v[208:211], v154 offset:54272
	ds_read_b128 v[212:215], v154 offset:55296
	ds_read_b128 v[216:219], v154 offset:56320
	global_load_lds_dwordx4 v[148:149], off
	s_add_i32 m0, s28, 0x2000
	s_add_u32 s20, s20, 0x40080
	v_lshl_add_u64 v[148:149], v[220:221], 0, s[10:11]
	s_addc_u32 s21, s21, 0
	s_add_i32 s28, vcc_lo, s40
	global_load_lds_dwordx4 v[148:149], off
	v_lshl_add_u64 v[148:149], s[20:21], 0, v[130:131]
	s_mov_b32 m0, s28
	s_nop 0
	global_load_lds_dwordx4 v[148:149], off
	v_lshl_add_u64 v[148:149], s[20:21], 0, v[134:135]
	s_add_i32 m0, s28, 0x2000
	s_nop 0
	global_load_lds_dwordx4 v[148:149], off
	v_lshl_add_u64 v[148:149], v[222:223], 0, s[10:11]
	s_mov_b32 m0, s73
	s_nop 0
	global_load_lds_dwordx4 v[148:149], off
	v_lshl_add_u64 v[148:149], v[224:225], 0, s[10:11]
	s_mov_b32 m0, s74
	s_nop 0
	global_load_lds_dwordx4 v[148:149], off
	s_waitcnt vmcnt(8)
	s_waitcnt lgkmcnt(0)
	s_barrier
	s_setprio 1
	s_waitcnt lgkmcnt(0)
	v_mfma_f32_16x16x32_bf16 v[60:63], v[156:159], v[188:191], v[60:63]
	v_mfma_f32_16x16x32_bf16 v[56:59], v[164:167], v[188:191], v[56:59]
	v_mfma_f32_16x16x32_bf16 v[52:55], v[156:159], v[196:199], v[52:55]
	v_mfma_f32_16x16x32_bf16 v[44:47], v[164:167], v[196:199], v[44:47]
	v_mfma_f32_16x16x32_bf16 v[36:39], v[156:159], v[204:207], v[36:39]
	v_mfma_f32_16x16x32_bf16 v[28:31], v[164:167], v[204:207], v[28:31]
	v_mfma_f32_16x16x32_bf16 v[20:23], v[156:159], v[212:215], v[20:23]
	v_mfma_f32_16x16x32_bf16 v[12:15], v[164:167], v[212:215], v[12:15]
	v_mfma_f32_16x16x32_bf16 v[60:63], v[160:163], v[192:195], v[60:63]
	v_mfma_f32_16x16x32_bf16 v[56:59], v[168:171], v[192:195], v[56:59]
	v_mfma_f32_16x16x32_bf16 v[52:55], v[160:163], v[200:203], v[52:55]
	v_mfma_f32_16x16x32_bf16 v[44:47], v[168:171], v[200:203], v[44:47]
	v_mfma_f32_16x16x32_bf16 v[36:39], v[160:163], v[208:211], v[36:39]
	v_mfma_f32_16x16x32_bf16 v[28:31], v[168:171], v[208:211], v[28:31]
	v_mfma_f32_16x16x32_bf16 v[20:23], v[160:163], v[216:219], v[20:23]
	v_mfma_f32_16x16x32_bf16 v[12:15], v[168:171], v[216:219], v[12:15]
	s_setprio 0
	s_setprio 1
	v_mfma_f32_16x16x32_bf16 v[48:51], v[172:175], v[188:191], v[48:51]
	v_mfma_f32_16x16x32_bf16 v[40:43], v[180:183], v[188:191], v[40:43]
	v_mfma_f32_16x16x32_bf16 v[32:35], v[172:175], v[196:199], v[32:35]
	v_mfma_f32_16x16x32_bf16 v[24:27], v[180:183], v[196:199], v[24:27]
	v_mfma_f32_16x16x32_bf16 v[16:19], v[172:175], v[204:207], v[16:19]
	v_mfma_f32_16x16x32_bf16 v[8:11], v[180:183], v[204:207], v[8:11]
	v_mfma_f32_16x16x32_bf16 v[4:7], v[172:175], v[212:215], v[4:7]
	v_mfma_f32_16x16x32_bf16 v[0:3], v[180:183], v[212:215], v[0:3]
	v_mfma_f32_16x16x32_bf16 v[48:51], v[176:179], v[192:195], v[48:51]
	v_mfma_f32_16x16x32_bf16 v[40:43], v[184:187], v[192:195], v[40:43]
	v_mfma_f32_16x16x32_bf16 v[32:35], v[176:179], v[200:203], v[32:35]
	v_mfma_f32_16x16x32_bf16 v[24:27], v[184:187], v[200:203], v[24:27]
	v_mfma_f32_16x16x32_bf16 v[16:19], v[176:179], v[208:211], v[16:19]
	v_mfma_f32_16x16x32_bf16 v[8:11], v[184:187], v[208:211], v[8:11]
	v_mfma_f32_16x16x32_bf16 v[4:7], v[176:179], v[216:219], v[4:7]
	v_mfma_f32_16x16x32_bf16 v[0:3], v[184:187], v[216:219], v[0:3]
	s_setprio 0
	s_barrier
	s_add_i32 s97, s97, 2
	s_add_u32 s26, s26, 0x100
	s_addc_u32 s27, s27, 0
	s_add_u32 s95, s95, 0x100
	s_addc_u32 s96, s96, 0
	s_cmp_gt_u32 s97, 13
	s_cbranch_scc0 .LBB0_123
	s_and_b64 vcc, exec, s[12:13]
	s_cbranch_vccz .LBB0_126
	s_barrier
.LBB0_126:
	v_lshl_add_u32 v148, s24, 8, v147
	v_or_b32_e32 v160, 16, v148
	v_ashrrev_i32_e32 v149, 31, v148
	v_ashrrev_i32_e32 v161, 31, v160
	v_or_b32_e32 v164, 32, v148
	v_lshl_add_u64 v[156:157], v[148:149], 2, s[8:9]
	v_lshl_add_u64 v[162:163], v[160:161], 2, s[8:9]
	v_ashrrev_i32_e32 v165, 31, v164
	v_or_b32_e32 v168, 48, v148
	v_mov_b32_e32 v158, v238
	v_lshl_add_u64 v[166:167], v[164:165], 2, s[8:9]
	v_mov_b32_e32 v162, v239
	v_ashrrev_i32_e32 v169, 31, v168
	v_mov_b32_e32 v166, v240
	v_lshl_add_u64 v[170:171], v[168:169], 2, s[8:9]
	v_mov_b32_e32 v170, v241
	s_nop 0
	v_mov_b32_e32 v172, v242
	v_mov_b32_e32 v174, v243
	v_mov_b32_e32 v176, v244
	v_mov_b32_e32 v146, v245
	s_ashr_i32 s20, s81, 1
	s_ashr_i32 s21, s20, 31
	s_lshl_b64 s[20:21], s[20:21], 25
	s_add_u32 s20, s0, s20
	s_addc_u32 s21, s1, s21
	s_lshl_b32 s15, s81, 8
	s_and_b32 s15, s15, 0x100
	v_or_b32_e32 v136, s15, v151
	v_lshlrev_b32_e32 v136, 1, v136
	v_lshlrev_b64 v[148:149], 10, v[148:149]
	v_lshlrev_b64 v[160:161], 10, v[160:161]
	v_lshl_add_u64 v[156:157], s[20:21], 0, v[136:137]
	v_lshlrev_b64 v[164:165], 10, v[164:165]
	v_lshl_add_u64 v[148:149], v[156:157], 0, v[148:149]
	v_lshl_add_u64 v[160:161], v[156:157], 0, v[160:161]
	v_lshl_add_u64 v[164:165], v[156:157], 0, v[164:165]
	s_mov_b32 s15, 0x20000
	s_mov_b64 s[20:21], 0x20000
	s_waitcnt vmcnt(0)
	v_pk_mul_f32 v[126:127], v[126:127], v[158:159] op_sel_hi:[1,0]
	v_pk_mul_f32 v[124:125], v[124:125], v[158:159] op_sel_hi:[1,0]
	v_pk_mul_f32 v[122:123], v[122:123], v[158:159] op_sel_hi:[1,0]
	v_pk_mul_f32 v[120:121], v[120:121], v[158:159] op_sel_hi:[1,0]
	v_pk_mul_f32 v[118:119], v[118:119], v[162:163] op_sel_hi:[1,0]
	v_pk_mul_f32 v[116:117], v[116:117], v[162:163] op_sel_hi:[1,0]
	v_pk_mul_f32 v[114:115], v[114:115], v[162:163] op_sel_hi:[1,0]
	v_pk_mul_f32 v[112:113], v[112:113], v[162:163] op_sel_hi:[1,0]
	v_pk_mul_f32 v[110:111], v[110:111], v[158:159] op_sel_hi:[1,0]
	v_pk_mul_f32 v[108:109], v[108:109], v[158:159] op_sel_hi:[1,0]
	v_pk_mul_f32 v[178:179], v[106:107], v[158:159] op_sel_hi:[1,0]
	v_pk_mul_f32 v[158:159], v[104:105], v[158:159] op_sel_hi:[1,0]
	v_cvt_pk_bf16_f32 v104, v124, v125
	v_cvt_pk_bf16_f32 v105, v126, v127
	v_cvt_pk_bf16_f32 v106, v120, v121
	v_cvt_pk_bf16_f32 v107, v122, v123
	v_pk_mul_f32 v[94:95], v[94:95], v[162:163] op_sel_hi:[1,0]
	v_pk_mul_f32 v[92:93], v[92:93], v[162:163] op_sel_hi:[1,0]
	v_pk_mul_f32 v[90:91], v[90:91], v[162:163] op_sel_hi:[1,0]
	v_pk_mul_f32 v[88:89], v[88:89], v[162:163] op_sel_hi:[1,0]
	v_pk_mul_f32 v[102:103], v[102:103], v[166:167] op_sel_hi:[1,0]
	v_pk_mul_f32 v[100:101], v[100:101], v[166:167] op_sel_hi:[1,0]
	v_pk_mul_f32 v[98:99], v[98:99], v[166:167] op_sel_hi:[1,0]
	v_pk_mul_f32 v[96:97], v[96:97], v[166:167] op_sel_hi:[1,0]
	v_pk_mul_f32 v[124:125], v[82:83], v[166:167] op_sel_hi:[1,0]
	v_pk_mul_f32 v[126:127], v[80:81], v[166:167] op_sel_hi:[1,0]
	v_cvt_pk_bf16_f32 v80, v116, v117
	v_cvt_pk_bf16_f32 v81, v118, v119
	v_cvt_pk_bf16_f32 v82, v112, v113
	v_cvt_pk_bf16_f32 v83, v114, v115
	v_cvt_pk_bf16_f32 v108, v108, v109
	v_cvt_pk_bf16_f32 v109, v110, v111
	v_cvt_pk_bf16_f32 v110, v158, v159
	v_cvt_pk_bf16_f32 v111, v178, v179
	v_pk_mul_f32 v[120:121], v[86:87], v[166:167] op_sel_hi:[1,0]
	v_pk_mul_f32 v[122:123], v[84:85], v[166:167] op_sel_hi:[1,0]
	global_store_dwordx4 v[148:149], v[104:107], off
	global_store_dwordx4 v[148:149], v[108:111], off offset:256
	v_cvt_pk_bf16_f32 v84, v92, v93
	v_cvt_pk_bf16_f32 v85, v94, v95
	v_cvt_pk_bf16_f32 v86, v88, v89
	v_cvt_pk_bf16_f32 v87, v90, v91
	v_cvt_pk_bf16_f32 v88, v100, v101
	v_cvt_pk_bf16_f32 v89, v102, v103
	v_cvt_pk_bf16_f32 v90, v96, v97
	v_cvt_pk_bf16_f32 v91, v98, v99
	global_store_dwordx4 v[160:161], v[80:83], off
	global_store_dwordx4 v[160:161], v[84:87], off offset:256
	global_store_dwordx4 v[164:165], v[88:91], off
	v_lshlrev_b64 v[80:81], 10, v[168:169]
	v_pk_mul_f32 v[78:79], v[78:79], v[170:171] op_sel_hi:[1,0]
	v_pk_mul_f32 v[76:77], v[76:77], v[170:171] op_sel_hi:[1,0]
	v_pk_mul_f32 v[82:83], v[74:75], v[170:171] op_sel_hi:[1,0]
	v_pk_mul_f32 v[74:75], v[72:73], v[170:171] op_sel_hi:[1,0]
	v_lshl_add_u64 v[80:81], v[156:157], 0, v[80:81]
	v_cvt_pk_bf16_f32 v72, v76, v77
	v_cvt_pk_bf16_f32 v73, v78, v79
	v_cvt_pk_bf16_f32 v74, v74, v75
	v_cvt_pk_bf16_f32 v75, v82, v83
	global_store_dwordx4 v[80:81], v[72:75], off
	v_pk_mul_f32 v[70:71], v[70:71], v[170:171] op_sel_hi:[1,0]
	v_pk_mul_f32 v[68:69], v[68:69], v[170:171] op_sel_hi:[1,0]
	v_pk_mul_f32 v[72:73], v[66:67], v[170:171] op_sel_hi:[1,0]
	v_pk_mul_f32 v[66:67], v[64:65], v[170:171] op_sel_hi:[1,0]
	v_cvt_pk_bf16_f32 v64, v68, v69
	v_cvt_pk_bf16_f32 v65, v70, v71
	v_cvt_pk_bf16_f32 v66, v66, v67
	v_cvt_pk_bf16_f32 v67, v72, v73
	v_pk_mul_f32 v[60:61], v[60:61], v[172:173] op_sel_hi:[1,0]
	global_store_dwordx4 v[80:81], v[64:67], off offset:256
	v_pk_mul_f32 v[62:63], v[62:63], v[172:173] op_sel_hi:[1,0]
	v_pk_mul_f32 v[50:51], v[50:51], v[172:173] op_sel_hi:[1,0]
	v_pk_mul_f32 v[66:67], v[58:59], v[172:173] op_sel_hi:[1,0]
	v_pk_mul_f32 v[58:59], v[56:57], v[172:173] op_sel_hi:[1,0]
	v_cvt_pk_bf16_f32 v56, v60, v61
	v_add_co_u32_e32 v60, vcc, s15, v148
	v_cvt_pk_bf16_f32 v57, v62, v63
	v_cvt_pk_bf16_f32 v58, v58, v59
	v_cvt_pk_bf16_f32 v59, v66, v67
	v_addc_co_u32_e32 v61, vcc, 0, v149, vcc
	global_store_dwordx4 v[60:61], v[56:59], off
	v_pk_mul_f32 v[48:49], v[48:49], v[172:173] op_sel_hi:[1,0]
	v_lshl_add_u64 v[64:65], v[148:149], 0, s[20:21]
	v_pk_mul_f32 v[56:57], v[42:43], v[172:173] op_sel_hi:[1,0]
	v_pk_mul_f32 v[42:43], v[40:41], v[172:173] op_sel_hi:[1,0]
	v_cvt_pk_bf16_f32 v40, v48, v49
	v_cvt_pk_bf16_f32 v41, v50, v51
	v_cvt_pk_bf16_f32 v42, v42, v43
	v_cvt_pk_bf16_f32 v43, v56, v57
	global_store_dwordx4 v[64:65], v[40:43], off offset:256
	v_pk_mul_f32 v[44:45], v[44:45], v[174:175] op_sel_hi:[1,0]
	s_mov_b32 s15, 0x24000
	v_pk_mul_f32 v[42:43], v[54:55], v[174:175] op_sel_hi:[1,0]
	v_pk_mul_f32 v[40:41], v[52:53], v[174:175] op_sel_hi:[1,0]
	v_pk_mul_f32 v[46:47], v[46:47], v[174:175] op_sel_hi:[1,0]
	v_cvt_pk_bf16_f32 v40, v40, v41
	v_cvt_pk_bf16_f32 v41, v42, v43
	v_cvt_pk_bf16_f32 v42, v44, v45
	v_add_co_u32_e32 v44, vcc, s15, v148
	v_cvt_pk_bf16_f32 v43, v46, v47
	s_nop 0
	v_addc_co_u32_e32 v45, vcc, 0, v149, vcc
	s_mov_b64 s[20:21], 0x24000
	global_store_dwordx4 v[44:45], v[40:43], off
	v_pk_mul_f32 v[34:35], v[34:35], v[174:175] op_sel_hi:[1,0]
	v_pk_mul_f32 v[32:33], v[32:33], v[174:175] op_sel_hi:[1,0]
	v_pk_mul_f32 v[40:41], v[26:27], v[174:175] op_sel_hi:[1,0]
	v_pk_mul_f32 v[26:27], v[24:25], v[174:175] op_sel_hi:[1,0]
	v_lshl_add_u64 v[48:49], v[148:149], 0, s[20:21]
	v_cvt_pk_bf16_f32 v24, v32, v33
	v_cvt_pk_bf16_f32 v25, v34, v35
	v_cvt_pk_bf16_f32 v26, v26, v27
	v_cvt_pk_bf16_f32 v27, v40, v41
	global_store_dwordx4 v[48:49], v[24:27], off offset:256
	v_pk_mul_f32 v[28:29], v[28:29], v[176:177] op_sel_hi:[1,0]
	s_mov_b32 s15, 0x28000
	v_pk_mul_f32 v[26:27], v[38:39], v[176:177] op_sel_hi:[1,0]
	v_pk_mul_f32 v[24:25], v[36:37], v[176:177] op_sel_hi:[1,0]
	v_pk_mul_f32 v[30:31], v[30:31], v[176:177] op_sel_hi:[1,0]
	v_cvt_pk_bf16_f32 v24, v24, v25
	v_cvt_pk_bf16_f32 v25, v26, v27
	v_cvt_pk_bf16_f32 v26, v28, v29
	v_add_co_u32_e32 v28, vcc, s15, v148
	v_cvt_pk_bf16_f32 v27, v30, v31
	s_nop 0
	v_addc_co_u32_e32 v29, vcc, 0, v149, vcc
	s_mov_b64 s[20:21], 0x28000
	global_store_dwordx4 v[28:29], v[24:27], off
	v_pk_mul_f32 v[18:19], v[18:19], v[176:177] op_sel_hi:[1,0]
	v_pk_mul_f32 v[16:17], v[16:17], v[176:177] op_sel_hi:[1,0]
	v_pk_mul_f32 v[24:25], v[10:11], v[176:177] op_sel_hi:[1,0]
	v_pk_mul_f32 v[10:11], v[8:9], v[176:177] op_sel_hi:[1,0]
	v_lshl_add_u64 v[32:33], v[148:149], 0, s[20:21]
	v_cvt_pk_bf16_f32 v8, v16, v17
	v_cvt_pk_bf16_f32 v9, v18, v19
	v_cvt_pk_bf16_f32 v10, v10, v11
	v_cvt_pk_bf16_f32 v11, v24, v25
	global_store_dwordx4 v[32:33], v[8:11], off offset:256
	v_pk_mul_f32 v[12:13], v[12:13], v[146:147] op_sel_hi:[1,0]
	s_mov_b32 s15, 0x2c000
	v_pk_mul_f32 v[10:11], v[22:23], v[146:147] op_sel_hi:[1,0]
	v_pk_mul_f32 v[8:9], v[20:21], v[146:147] op_sel_hi:[1,0]
	v_pk_mul_f32 v[14:15], v[14:15], v[146:147] op_sel_hi:[1,0]
	v_cvt_pk_bf16_f32 v8, v8, v9
	v_cvt_pk_bf16_f32 v9, v10, v11
	v_cvt_pk_bf16_f32 v10, v12, v13
	v_add_co_u32_e32 v12, vcc, s15, v148
	v_cvt_pk_bf16_f32 v11, v14, v15
	s_nop 0
	v_addc_co_u32_e32 v13, vcc, 0, v149, vcc
	s_mov_b64 s[20:21], 0x2c000
	global_store_dwordx4 v[12:13], v[8:11], off
	v_pk_mul_f32 v[6:7], v[6:7], v[146:147] op_sel_hi:[1,0]
	v_pk_mul_f32 v[4:5], v[4:5], v[146:147] op_sel_hi:[1,0]
	v_pk_mul_f32 v[8:9], v[2:3], v[146:147] op_sel_hi:[1,0]
	v_pk_mul_f32 v[2:3], v[0:1], v[146:147] op_sel_hi:[1,0]
	v_cvt_pk_bf16_f32 v92, v122, v123
	v_cvt_pk_bf16_f32 v93, v120, v121
	v_cvt_pk_bf16_f32 v94, v126, v127
	v_cvt_pk_bf16_f32 v95, v124, v125
	v_lshl_add_u64 v[16:17], v[148:149], 0, s[20:21]
	v_cvt_pk_bf16_f32 v0, v4, v5
	v_cvt_pk_bf16_f32 v1, v6, v7
	v_cvt_pk_bf16_f32 v2, v2, v3
	v_cvt_pk_bf16_f32 v3, v8, v9
	s_andn2_b64 vcc, exec, s[2:3]
	s_mov_b64 s[2:3], -1
	global_store_dwordx4 v[164:165], v[92:95], off offset:256
	global_store_dwordx4 v[16:17], v[0:3], off offset:256
	s_cbranch_vccnz .LBB0_119
	s_andn2_b64 vcc, exec, s[6:7]
	s_cbranch_vccnz .LBB0_118
	s_barrier
	s_branch .LBB0_118

.LBB0_416:
	s_waitcnt vmcnt(0)
	v_readfirstlane_b32 s12, v78
	s_nop 1
	v_mov_b32_e32 v1, s12
	s_mov_b64 s[10:11], 0

.LBB0_418:
	v_readfirstlane_b32 s0, v1
	s_cmpk_gt_i32 s0, 0xa8f
	s_mov_b64 s[10:11], -1
	s_cbranch_scc1 .LBB0_417
	v_mov_b32_e32 v1, 0
	s_and_saveexec_b64 s[10:11], s[2:3]
	s_cbranch_execz .LBB0_423
	s_mov_b64 s[14:15], exec
	v_mbcnt_lo_u32_b32 v1, s14, 0
	v_mbcnt_hi_u32_b32 v1, s15, v1
	v_cmp_eq_u32_e32 vcc, 0, v1
	s_and_saveexec_b64 s[12:13], vcc
	s_cbranch_execz .LBB0_422
	s_bcnt1_i32_b64 s14, s[14:15]
	v_mov_b32_e32 v2, s14
	global_atomic_add v78, v3, v2, s[88:89] offset:256 sc0
.LBB0_422:
	s_or_b64 exec, exec, s[12:13]
.LBB0_423:
	s_or_b64 exec, exec, s[10:11]
	s_lshl_b32 s12, s0, 3
	v_lshl_add_u32 v14, s0, 11, v28
	v_lshl_add_u32 v16, s0, 12, v29
	s_lshl_b32 s13, s0, 8
	s_lshl_b32 s14, s0, 4
	s_lshl_b32 s15, s0, 5
	s_mov_b32 s23, 0
	s_branch .LBB0_425
